# speedup vs baseline: 1.0543x; 1.0101x over previous
.LBB0_11:
	s_andn2_b64 vcc, exec, s[2:3]
	s_cbranch_vccnz .LBB0_23
	v_add_u32_e32 v18, 0xfffffc00, v77
	v_lshrrev_b32_e32 v2, 3, v18
	v_and_b32_e32 v20, 0x1fffffc0, v2
	v_mov_b32_e32 v21, 0
	v_lshlrev_b64 v[2:3], 14, v[20:21]
	v_lshlrev_b32_e32 v4, 7, v18
	s_waitcnt lgkmcnt(0)
	v_lshl_add_u64 v[2:3], s[4:5], 0, v[2:3]
	v_and_b32_e32 v20, 0x3f80, v4
	v_lshl_add_u64 v[2:3], v[2:3], 0, v[20:21]
	v_mov_b32_e32 v37, v21
	v_lshl_add_u64 v[2:3], v[2:3], 0, v[36:37]
	v_mov_b32_e32 v35, v21
	v_lshl_add_u64 v[2:3], v[2:3], 0, v[34:35]
	s_movk_i32 s10, 0x4000
	v_add_co_u32_e32 v4, vcc, s10, v2
	s_mov_b32 s10, 0x8000
	s_nop 0
	v_addc_co_u32_e32 v5, vcc, 0, v3, vcc
	v_add_co_u32_e32 v6, vcc, s10, v2
	s_mov_b32 s10, 0xc000
	s_nop 0
	v_addc_co_u32_e32 v7, vcc, 0, v3, vcc
	v_add_co_u32_e32 v8, vcc, s10, v2
	s_mov_b32 s10, 0x10000
	s_nop 0
	v_addc_co_u32_e32 v9, vcc, 0, v3, vcc
	v_add_co_u32_e32 v10, vcc, s10, v2
	s_mov_b32 s10, 0x14000
	s_nop 0
	v_addc_co_u32_e32 v11, vcc, 0, v3, vcc
	v_add_co_u32_e32 v12, vcc, s10, v2
	s_mov_b32 s10, 0x18000
	s_nop 0
	v_addc_co_u32_e32 v13, vcc, 0, v3, vcc
	v_add_co_u32_e32 v14, vcc, s10, v2
	s_mov_b32 s10, 0x1c000
	s_nop 0
	v_addc_co_u32_e32 v15, vcc, 0, v3, vcc
	v_add_co_u32_e32 v16, vcc, s10, v2
	s_mov_b32 s10, 0x40000
	s_nop 0
	v_addc_co_u32_e32 v17, vcc, 0, v3, vcc
	s_load_dwordx2 s[2:3], s[0:1], 0x20
	s_load_dwordx2 s[8:9], s[0:1], 0x10
	s_load_dwordx2 s[14:15], s[0:1], 0x28
	s_load_dwordx2 s[16:17], s[0:1], 0x18
	global_load_dword v44, v[2:3], off
	global_load_dword v43, v[4:5], off
	global_load_dword v42, v[6:7], off
	global_load_dword v41, v[8:9], off
	global_load_dword v40, v[10:11], off
	global_load_dword v38, v[12:13], off
	global_load_dword v19, v[14:15], off
	global_load_dword v39, v[16:17], off
	v_add_co_u32_e32 v4, vcc, s10, v2
	s_mov_b32 s10, 0x44000
	s_nop 0
	v_addc_co_u32_e32 v5, vcc, 0, v3, vcc
	v_add_co_u32_e32 v6, vcc, s10, v2
	s_mov_b32 s10, 0x48000
	s_nop 0
	v_addc_co_u32_e32 v7, vcc, 0, v3, vcc
	v_add_co_u32_e32 v8, vcc, s10, v2
	s_mov_b32 s10, 0x4c000
	s_nop 0
	v_addc_co_u32_e32 v9, vcc, 0, v3, vcc
	v_add_co_u32_e32 v10, vcc, s10, v2
	s_mov_b32 s10, 0x50000
	s_nop 0
	v_addc_co_u32_e32 v11, vcc, 0, v3, vcc
	v_add_co_u32_e32 v12, vcc, s10, v2
	s_mov_b32 s10, 0x54000
	s_nop 0
	v_addc_co_u32_e32 v13, vcc, 0, v3, vcc
	v_add_co_u32_e32 v14, vcc, s10, v2
	s_mov_b32 s10, 0x58000
	s_nop 0
	v_addc_co_u32_e32 v15, vcc, 0, v3, vcc
	v_add_co_u32_e32 v16, vcc, s10, v2
	s_mov_b32 s10, 0x5c000
	s_nop 0
	v_addc_co_u32_e32 v17, vcc, 0, v3, vcc
	v_add_co_u32_e32 v22, vcc, s10, v2
	s_mov_b32 s10, 0x80000
	s_nop 0
	v_addc_co_u32_e32 v23, vcc, 0, v3, vcc
	global_load_dword v52, v[4:5], off
	global_load_dword v51, v[6:7], off
	global_load_dword v50, v[8:9], off
	global_load_dword v49, v[10:11], off
	global_load_dword v48, v[12:13], off
	global_load_dword v46, v[14:15], off
	global_load_dword v45, v[16:17], off
	global_load_dword v47, v[22:23], off
	v_add_co_u32_e32 v4, vcc, s10, v2
	s_mov_b32 s10, 0x84000
	s_nop 0
	v_addc_co_u32_e32 v5, vcc, 0, v3, vcc
	v_add_co_u32_e32 v6, vcc, s10, v2
	s_mov_b32 s10, 0x88000
	s_nop 0
	v_addc_co_u32_e32 v7, vcc, 0, v3, vcc
	v_add_co_u32_e32 v8, vcc, s10, v2
	s_mov_b32 s10, 0x8c000
	s_nop 0
	v_addc_co_u32_e32 v9, vcc, 0, v3, vcc
	v_add_co_u32_e32 v10, vcc, s10, v2
	s_mov_b32 s10, 0x90000
	s_nop 0
	v_addc_co_u32_e32 v11, vcc, 0, v3, vcc
	v_add_co_u32_e32 v12, vcc, s10, v2
	s_mov_b32 s10, 0x94000
	s_nop 0
	v_addc_co_u32_e32 v13, vcc, 0, v3, vcc
	v_add_co_u32_e32 v14, vcc, s10, v2
	s_mov_b32 s10, 0x98000
	s_nop 0
	v_addc_co_u32_e32 v15, vcc, 0, v3, vcc
	v_add_co_u32_e32 v16, vcc, s10, v2
	s_mov_b32 s10, 0x9c000
	s_nop 0
	v_addc_co_u32_e32 v17, vcc, 0, v3, vcc
	v_add_co_u32_e32 v22, vcc, s10, v2
	s_mov_b32 s10, 0xc0000
	s_nop 0
	v_addc_co_u32_e32 v23, vcc, 0, v3, vcc
	global_load_dword v60, v[4:5], off
	global_load_dword v59, v[6:7], off
	global_load_dword v58, v[8:9], off
	global_load_dword v57, v[10:11], off
	global_load_dword v56, v[12:13], off
	global_load_dword v54, v[14:15], off
	global_load_dword v53, v[16:17], off
	global_load_dword v55, v[22:23], off
	v_add_co_u32_e32 v4, vcc, s10, v2
	s_mov_b32 s10, 0xc4000
	s_nop 0
	v_addc_co_u32_e32 v5, vcc, 0, v3, vcc
	v_add_co_u32_e32 v6, vcc, s10, v2
	s_mov_b32 s10, 0xc8000
	s_nop 0
	v_addc_co_u32_e32 v7, vcc, 0, v3, vcc
	v_add_co_u32_e32 v8, vcc, s10, v2
	s_mov_b32 s10, 0xcc000
	s_nop 0
	v_addc_co_u32_e32 v9, vcc, 0, v3, vcc
	v_add_co_u32_e32 v10, vcc, s10, v2
	s_mov_b32 s10, 0xd0000
	s_nop 0
	v_addc_co_u32_e32 v11, vcc, 0, v3, vcc
	v_add_co_u32_e32 v12, vcc, s10, v2
	s_mov_b32 s10, 0xd4000
	s_nop 0
	v_addc_co_u32_e32 v13, vcc, 0, v3, vcc
	v_add_co_u32_e32 v14, vcc, s10, v2
	s_mov_b32 s10, 0xd8000
	s_nop 0
	v_addc_co_u32_e32 v15, vcc, 0, v3, vcc
	v_add_co_u32_e32 v16, vcc, s10, v2
	s_mov_b32 s10, 0xdc000
	s_nop 0
	v_addc_co_u32_e32 v17, vcc, 0, v3, vcc
	v_add_co_u32_e32 v2, vcc, s10, v2
	v_bfe_u32 v69, v18, 7, 2
	s_nop 0
	v_addc_co_u32_e32 v3, vcc, 0, v3, vcc
	v_lshlrev_b32_e32 v20, 14, v69
	global_load_dword v68, v[4:5], off
	global_load_dword v67, v[6:7], off
	global_load_dword v66, v[8:9], off
	global_load_dword v65, v[10:11], off
	global_load_dword v64, v[12:13], off
	global_load_dword v62, v[14:15], off
	global_load_dword v61, v[16:17], off
	global_load_dword v63, v[2:3], off
	s_waitcnt lgkmcnt(0)
	v_lshl_add_u64 v[2:3], s[8:9], 0, v[20:21]
	v_lshlrev_b32_e32 v20, 4, v0
	v_lshlrev_b32_e32 v4, 12, v69
	v_lshl_add_u64 v[70:71], v[2:3], 0, v[20:21]
	s_movk_i32 s8, 0x2000
	v_add_co_u32_e32 v72, vcc, s8, v70
	v_lshl_or_b32 v2, v76, 10, v4
	s_nop 0
	v_addc_co_u32_e32 v73, vcc, 0, v71, vcc
	s_movk_i32 s8, 0x3000
	v_or_b32_e32 v3, v2, v1
	v_add_co_u32_e32 v78, vcc, s8, v70
	v_lshlrev_b32_e32 v77, 2, v3
	v_or_b32_e32 v2, v2, v0
	v_mov_b32_e32 v3, 0xf00
	v_addc_co_u32_e32 v79, vcc, 0, v71, vcc
	global_load_dword v26, v77, s[2:3]
	global_load_dword v27, v77, s[2:3] offset:256
	global_load_dword v28, v77, s[2:3] offset:512
	global_load_dword v29, v77, s[2:3] offset:768
	global_load_dword v22, v77, s[2:3] offset:1024
	global_load_dword v23, v77, s[2:3] offset:1280
	global_load_dword v24, v77, s[2:3] offset:1536
	global_load_dword v25, v77, s[2:3] offset:1792
	v_lshl_or_b32 v80, v2, 2, v3
	global_load_dword v34, v77, s[2:3] offset:2048
	global_load_dword v35, v77, s[2:3] offset:2304
	global_load_dword v36, v77, s[2:3] offset:2560
	global_load_dword v37, v77, s[2:3] offset:2816
	global_load_dword v30, v77, s[2:3] offset:3072
	global_load_dword v31, v77, s[2:3] offset:3328
	global_load_dword v32, v77, s[2:3] offset:3584
	global_load_dword v33, v80, s[2:3]
	global_load_dwordx4 v[10:13], v[72:73], off offset:-4096
	global_load_dwordx4 v[6:9], v[72:73], off
	global_load_dwordx4 v[14:17], v[70:71], off
	global_load_dwordx4 v[2:5], v[78:79], off
	s_load_dwordx2 s[8:9], s[0:1], 0x48
	s_load_dwordx2 s[26:27], s[0:1], 0x50
	s_load_dwordx2 s[28:29], s[0:1], 0x60
	s_load_dwordx2 s[30:31], s[0:1], 0x68
	v_cmp_gt_u32_e32 vcc, 32, v0
	v_mov_b32_e32 v71, v21
	v_mov_b32_e32 v72, v21
	v_mov_b32_e32 v73, v21
	s_and_saveexec_b64 s[10:11], vcc
	s_cbranch_execz .LBB0_14
	v_cmp_gt_u32_e64 s[2:3], 16, v0
	v_lshlrev_b32_e32 v21, 2, v0
	v_lshlrev_b32_e32 v69, 6, v69
	v_mov_b32_e32 v70, s15
	v_mov_b32_e32 v71, s17
	v_cndmask_b32_e64 v71, v70, v71, s[2:3]
	v_mov_b32_e32 v70, s14
	v_mov_b32_e32 v72, s16
	v_cndmask_b32_e64 v70, v70, v72, s[2:3]
	v_lshlrev_b32_e32 v72, 2, v69
	v_mov_b32_e32 v73, 0
	v_and_b32_e32 v21, 60, v21
	v_lshl_add_u64 v[70:71], v[70:71], 0, v[72:73]
	v_lshlrev_b32_e32 v72, 2, v21
	v_lshl_add_u64 v[70:71], v[70:71], 0, v[72:73]
	global_load_dwordx4 v[70:73], v[70:71], off
	s_waitcnt vmcnt(0)
	v_mov_b32_e32 v21, v70
.LBB0_14:
	s_or_b64 exec, exec, s[10:11]
	v_lshlrev_b32_e32 v70, 3, v0
	v_and_b32_e32 v70, 0x78, v70
	v_or_b32_e32 v70, 0x2400, v70
	s_waitcnt vmcnt(1)
	v_cvt_pk_bf16_f32 v14, v14, v15
	v_cvt_pk_bf16_f32 v15, v16, v17
	v_lshrrev_b32_e32 v16, 4, v0
	s_movk_i32 s10, 0x90
	v_mad_u32_u24 v16, v16, s10, v70
	ds_write_b64 v16, v[14:15]
	v_or_b32_e32 v14, 0x100, v0
	v_cvt_pk_bf16_f32 v10, v10, v11
	v_cvt_pk_bf16_f32 v11, v12, v13
	v_lshrrev_b32_e32 v12, 4, v14
	v_mad_u32_u24 v12, v12, s10, v70
	ds_write_b64 v12, v[10:11]
	v_or_b32_e32 v10, 0x200, v0
	v_cvt_pk_bf16_f32 v6, v6, v7
	v_cvt_pk_bf16_f32 v7, v8, v9
	v_lshrrev_b32_e32 v8, 4, v10
	v_mad_u32_u24 v8, v8, s10, v70
	ds_write_b64 v8, v[6:7]
	v_or_b32_e32 v6, 0x300, v0
	s_waitcnt vmcnt(0)
	v_cvt_pk_bf16_f32 v2, v2, v3
	v_cvt_pk_bf16_f32 v3, v4, v5
	v_lshrrev_b32_e32 v4, 4, v6
	v_mad_u32_u24 v4, v4, s10, v70
	v_lshlrev_b32_e32 v6, 5, v76
	ds_write_b64 v4, v[2:3]
	v_cvt_pk_bf16_f32 v2, v26, v27
	v_cvt_pk_bf16_f32 v3, v28, v29
	v_cvt_pk_bf16_f32 v4, v34, v35
	v_cvt_pk_bf16_f32 v5, v36, v37
	v_mad_u32_u24 v6, v1, s10, v6
	v_lshlrev_b32_e32 v69, 5, v18
	ds_write_b128 v6, v[2:5]
	v_cvt_pk_bf16_f32 v2, v22, v23
	v_cvt_pk_bf16_f32 v3, v24, v25
	v_cvt_pk_bf16_f32 v4, v30, v31
	v_cvt_pk_bf16_f32 v5, v32, v33
	ds_write_b128 v6, v[2:5] offset:16
	s_and_saveexec_b64 s[2:3], vcc
	v_mov_b32_e32 v70, v21
	ds_write_b128 v20, v[70:73] offset:18432
	s_or_b64 exec, exec, s[2:3]
	v_lshlrev_b32_e32 v71, 4, v75
	v_mad_u32_u24 v75, v74, s10, v71
	s_waitcnt lgkmcnt(0)
	s_barrier
	ds_read_b128 v[2:5], v75 offset:9216
	ds_read_b128 v[10:13], v75 offset:9248
	v_cvt_pk_bf16_f32 v6, v44, v43
	v_cvt_pk_bf16_f32 v7, v42, v41
	v_cvt_pk_bf16_f32 v8, v40, v38
	v_cvt_pk_bf16_f32 v9, v19, v39
	s_mov_b32 s2, 0x3fb8aa3b
	v_cmp_gt_u32_e32 vcc, 32, v1
	s_waitcnt lgkmcnt(1)
	v_mfma_f32_32x32x16_bf16 a[16:31], v[2:5], v[6:9], 0
	ds_read_b128 v[2:5], v75 offset:13824
	ds_read_b128 v[14:17], v75 offset:13856
	ds_read_b128 v[20:23], v75 offset:9312
	s_waitcnt lgkmcnt(2)
	v_mfma_f32_32x32x16_bf16 a[0:15], v[2:5], v[6:9], 0
	v_cvt_pk_bf16_f32 v2, v52, v51
	v_cvt_pk_bf16_f32 v3, v50, v49
	v_cvt_pk_bf16_f32 v4, v48, v46
	v_cvt_pk_bf16_f32 v5, v45, v47
	ds_read_b128 v[6:9], v75 offset:9280
	s_nop 0
	v_mfma_f32_32x32x16_bf16 a[16:31], v[10:13], v[2:5], a[16:31]
	v_cvt_pk_bf16_f32 v10, v60, v59
	v_cvt_pk_bf16_f32 v11, v58, v57
	v_cvt_pk_bf16_f32 v12, v56, v54
	v_cvt_pk_bf16_f32 v13, v53, v55
	s_waitcnt lgkmcnt(0)
	s_nop 0
	v_mfma_f32_32x32x16_bf16 a[16:31], v[6:9], v[10:13], a[16:31]
	v_cvt_pk_bf16_f32 v6, v68, v67
	v_cvt_pk_bf16_f32 v7, v66, v65
	v_cvt_pk_bf16_f32 v8, v64, v62
	v_cvt_pk_bf16_f32 v9, v61, v63
	s_nop 1
	v_mfma_f32_32x32x16_bf16 a[16:31], v[20:23], v[6:9], a[16:31]
	ds_read_b128 v[20:23], v75 offset:13888
	v_mfma_f32_32x32x16_bf16 a[0:15], v[14:17], v[2:5], a[0:15]
	ds_read_b128 v[2:5], v75 offset:13920
	s_nop 8
	v_accvgpr_read_b32 v37, a19
	v_accvgpr_read_b32 v36, a18
	v_accvgpr_read_b32 v35, a21
	s_waitcnt lgkmcnt(1)
	v_mfma_f32_32x32x16_bf16 a[0:15], v[20:23], v[10:13], a[0:15]
	v_accvgpr_read_b32 v21, a17
	v_accvgpr_read_b32 v20, a16
	v_accvgpr_read_b32 v34, a20
	v_accvgpr_read_b32 v33, a23
	v_accvgpr_read_b32 v32, a22
	v_accvgpr_read_b32 v31, a25
	v_accvgpr_read_b32 v30, a24
	s_waitcnt lgkmcnt(0)
	v_mfma_f32_32x32x16_bf16 a[0:15], v[2:5], v[6:9], a[0:15]
	ds_read_b128 v[6:9], v71 offset:18432
	ds_read_b128 v[10:13], v71 offset:18688
	ds_read_b128 v[14:17], v71 offset:18464
	v_accvgpr_read_b32 v29, a27
	v_accvgpr_read_b32 v28, a26
	v_accvgpr_read_b32 v25, a31
	s_waitcnt lgkmcnt(2)
	v_pk_add_f32 v[84:85], v[6:7], v[20:21]
	ds_read_b128 v[20:23], v71 offset:18720
	s_waitcnt lgkmcnt(2)
	v_fma_f32 v70, v84, v10, 0
	v_pk_add_f32 v[36:37], v[8:9], v[36:37]
	v_fmac_f32_e32 v70, v85, v11
	v_fmac_f32_e32 v70, v36, v12
	ds_read_b128 v[6:9], v71 offset:18496
	v_fmac_f32_e32 v70, v37, v13
	s_waitcnt lgkmcnt(2)
	v_pk_add_f32 v[34:35], v[14:15], v[34:35]
	ds_read_b128 v[10:13], v71 offset:18752
	s_waitcnt lgkmcnt(2)
	v_fmac_f32_e32 v70, v34, v20
	v_fmac_f32_e32 v70, v35, v21
	v_pk_add_f32 v[32:33], v[16:17], v[32:33]
	ds_read_b128 v[14:17], v71 offset:18528
	v_fmac_f32_e32 v70, v32, v22
	v_fmac_f32_e32 v70, v33, v23
	s_waitcnt lgkmcnt(2)
	v_pk_add_f32 v[86:87], v[6:7], v[30:31]
	v_pk_add_f32 v[88:89], v[8:9], v[28:29]
	s_waitcnt lgkmcnt(1)
	v_fmac_f32_e32 v70, v86, v10
	v_fmac_f32_e32 v70, v87, v11
	v_accvgpr_read_b32 v24, a30
	v_accvgpr_read_b32 v27, a29
	v_accvgpr_read_b32 v26, a28
	v_fmac_f32_e32 v70, v88, v12
	ds_read_b128 v[6:9], v71 offset:18784
	v_fmac_f32_e32 v70, v89, v13
	s_waitcnt lgkmcnt(1)
	v_pk_add_f32 v[90:91], v[14:15], v[26:27]
	v_pk_add_f32 v[92:93], v[16:17], v[24:25]
	ds_read_b128 v[10:13], v71 offset:18560
	ds_read_b128 v[14:17], v71 offset:18816
	v_accvgpr_read_b32 v21, a1
	v_accvgpr_read_b32 v83, a3
	v_accvgpr_read_b32 v82, a2
	v_accvgpr_read_b32 v20, a0
	s_waitcnt lgkmcnt(1)
	v_pk_add_f32 v[94:95], v[10:11], v[20:21]
	v_pk_add_f32 v[82:83], v[12:13], v[82:83]
	ds_read_b128 v[10:13], v75
	v_fmac_f32_e32 v70, v90, v6
	v_fmac_f32_e32 v70, v91, v7
	v_fmac_f32_e32 v70, v92, v8
	v_fmac_f32_e32 v70, v93, v9
	ds_read_b128 v[6:9], v71 offset:18592
	ds_read_b128 v[20:23], v71 offset:18848
	s_waitcnt lgkmcnt(3)
	v_fmac_f32_e32 v70, v94, v14
	v_fmac_f32_e32 v70, v95, v15
	v_fmac_f32_e32 v70, v82, v16
	ds_read_b128 v[24:27], v75 offset:4608
	ds_read_b128 v[28:31], v75 offset:32
	v_accvgpr_read_b32 v81, a5
	v_accvgpr_read_b32 v80, a4
	v_fmac_f32_e32 v70, v83, v17
	v_cvt_pk_bf16_f32 v14, v84, v85
	v_cvt_pk_bf16_f32 v15, v36, v37
	v_cvt_pk_bf16_f32 v16, v34, v35
	v_cvt_pk_bf16_f32 v17, v32, v33
	v_accvgpr_read_b32 v79, a7
	v_accvgpr_read_b32 v78, a6
	s_waitcnt lgkmcnt(4)
	v_mfma_f32_32x32x16_bf16 a[16:31], v[10:13], v[14:17], 0
	s_waitcnt lgkmcnt(3)
	v_add_f32_e64 v32, v6, v80
	v_add_f32_e64 v33, v7, v81
	v_add_f32_e64 v34, v8, v78
	v_add_f32_e64 v35, v9, v79
	s_waitcnt lgkmcnt(2)
	v_fmac_f32_e32 v70, v32, v20
	ds_read_b128 v[6:9], v75 offset:4640
	ds_read_b128 v[10:13], v71 offset:18880
	v_accvgpr_read_b32 v3, a15
	v_accvgpr_read_b32 v2, a14
	v_accvgpr_read_b32 v5, a13
	v_accvgpr_read_b32 v4, a12
	v_accvgpr_read_b32 v73, a11
	v_accvgpr_read_b32 v72, a10
	v_accvgpr_read_b32 v77, a9
	v_accvgpr_read_b32 v76, a8
	v_fmac_f32_e32 v70, v33, v21
	s_waitcnt lgkmcnt(3)
	v_mfma_f32_32x32x16_bf16 a[0:15], v[24:27], v[14:17], 0
	v_fmac_f32_e32 v70, v34, v22
	v_fmac_f32_e32 v70, v35, v23
	ds_read_b128 v[20:23], v71 offset:18624
	ds_read_b128 v[24:27], v71 offset:18656
	v_cvt_pk_bf16_f32 v14, v86, v87
	v_cvt_pk_bf16_f32 v15, v88, v89
	v_cvt_pk_bf16_f32 v16, v90, v91
	v_cvt_pk_bf16_f32 v17, v92, v93
	s_waitcnt lgkmcnt(1)
	v_pk_add_f32 v[36:37], v[20:21], v[76:77]
	v_pk_add_f32 v[72:73], v[22:23], v[72:73]
	v_mfma_f32_32x32x16_bf16 a[16:31], v[28:31], v[14:17], a[16:31]
	ds_read_b128 v[28:31], v71 offset:18912
	ds_read_b128 v[20:23], v75 offset:64
	v_fmac_f32_e32 v70, v36, v10
	v_fmac_f32_e32 v70, v37, v11
	v_fmac_f32_e32 v70, v72, v12
	v_fmac_f32_e32 v70, v73, v13
	v_mov_b32_e32 v76, 0
	v_mfma_f32_32x32x16_bf16 a[0:15], v[6:9], v[14:17], a[0:15]
	ds_read_b128 v[10:13], v75 offset:4672
	ds_read_b128 v[14:17], v75 offset:96
	v_cvt_pk_bf16_f32 v6, v94, v95
	v_cvt_pk_bf16_f32 v7, v82, v83
	v_cvt_pk_bf16_f32 v8, v32, v33
	v_cvt_pk_bf16_f32 v9, v34, v35
	v_mov_b32_e32 v77, 0
	v_mov_b32_e32 v78, 0
	s_waitcnt lgkmcnt(2)
	v_mfma_f32_32x32x16_bf16 a[16:31], v[20:23], v[6:9], a[16:31]
	v_add_f32_e64 v20, v24, v4
	v_add_f32_e64 v21, v25, v5
	v_add_f32_e64 v22, v26, v2
	v_add_f32_e64 v23, v27, v3
	ds_read_b128 v[2:5], v75 offset:4704
	v_fmac_f32_e32 v70, v20, v28
	v_fmac_f32_e32 v70, v21, v29
	v_fmac_f32_e32 v70, v22, v30
	v_fmac_f32_e32 v70, v23, v31
	s_waitcnt lgkmcnt(2)
	v_mfma_f32_32x32x16_bf16 a[0:15], v[10:13], v[6:9], a[0:15]
	v_cvt_pk_bf16_f32 v6, v36, v37
	v_cvt_pk_bf16_f32 v7, v72, v73
	v_cvt_pk_bf16_f32 v8, v20, v21
	v_cvt_pk_bf16_f32 v9, v22, v23
	v_mov_b32_e32 v79, 0
	v_mov_b32_e32 v71, v70
	s_nop 1
	v_permlane32_swap_b32_e32 v70, v71
	s_waitcnt lgkmcnt(1)
	v_mfma_f32_32x32x16_bf16 a[16:31], v[14:17], v[6:9], a[16:31]
	s_waitcnt lgkmcnt(0)
	v_mfma_f32_32x32x16_bf16 a[0:15], v[2:5], v[6:9], a[0:15]
	s_nop 9
	v_accvgpr_read_b32 v25, a31
	v_accvgpr_read_b32 v24, a30
	v_accvgpr_read_b32 v2, a16
	v_accvgpr_read_b32 v15, a21
	v_accvgpr_read_b32 v14, a20
	v_accvgpr_read_b32 v13, a25
	v_accvgpr_read_b32 v12, a24
	v_accvgpr_read_b32 v23, a29
	v_accvgpr_read_b32 v37, a9
	v_accvgpr_read_b32 v36, a8
	v_accvgpr_read_b32 v22, a28
	v_pk_mul_f32 v[4:5], v[24:25], s[2:3] op_sel_hi:[1,0]
	v_accvgpr_read_b32 v3, a17
	v_pk_mul_f32 v[24:25], v[36:37], s[2:3] op_sel_hi:[1,0]
	v_accvgpr_read_b32 v37, a1
	v_accvgpr_read_b32 v11, a19
	v_accvgpr_read_b32 v10, a18
	v_accvgpr_read_b32 v33, a5
	v_accvgpr_read_b32 v32, a4
	v_accvgpr_read_b32 v81, a13
	v_accvgpr_read_b32 v80, a12
	v_accvgpr_read_b32 v83, a15
	v_accvgpr_read_b32 v82, a14
	v_pk_mul_f32 v[6:7], v[22:23], s[2:3] op_sel_hi:[1,0]
	v_pk_mul_f32 v[12:13], v[12:13], s[2:3] op_sel_hi:[1,0]
	v_pk_mul_f32 v[22:23], v[14:15], s[2:3] op_sel_hi:[1,0]
	v_pk_mul_f32 v[30:31], v[2:3], s[2:3] op_sel_hi:[1,0]
	v_mov_b32_e32 v3, 0
	v_accvgpr_read_b32 v36, a0
	v_pk_mul_f32 v[26:27], v[10:11], s[2:3] op_sel_hi:[1,0]
	v_cvt_pk_fp8_f32 v76, v30, v31
	v_cvt_pk_fp8_f32 v77, v22, v23
	v_cvt_pk_fp8_f32 v78, v12, v13
	v_cvt_pk_fp8_f32 v79, v6, v7
	v_pk_mul_f32 v[10:11], v[82:83], s[2:3] op_sel_hi:[1,0]
	v_pk_mul_f32 v[14:15], v[80:81], s[2:3] op_sel_hi:[1,0]
	v_pk_mul_f32 v[32:33], v[32:33], s[2:3] op_sel_hi:[1,0]
	v_pk_mul_f32 v[36:37], v[36:37], s[2:3] op_sel_hi:[1,0]
	v_mov_b32_e32 v80, v3
	v_mov_b32_e32 v81, v3
	v_mov_b32_e32 v82, v3
	v_mov_b32_e32 v83, v3
	v_cvt_pk_fp8_f32 v80, v36, v37
	v_cvt_pk_fp8_f32 v81, v32, v33
	v_cvt_pk_fp8_f32 v82, v24, v25
	v_cvt_pk_fp8_f32 v83, v14, v15
	v_accvgpr_read_b32 v17, a23
	v_accvgpr_read_b32 v16, a22
	v_accvgpr_read_b32 v21, a27
	v_accvgpr_read_b32 v20, a26
	v_accvgpr_read_b32 v35, a3
	v_accvgpr_read_b32 v34, a2
	v_accvgpr_read_b32 v29, a7
	v_accvgpr_read_b32 v28, a6
	v_accvgpr_read_b32 v73, a11
	v_accvgpr_read_b32 v72, a10
	v_pk_mul_f32 v[8:9], v[20:21], s[2:3] op_sel_hi:[1,0]
	v_pk_mul_f32 v[16:17], v[16:17], s[2:3] op_sel_hi:[1,0]
	v_cvt_pk_fp8_f32 v76, v26, v27 op_sel:[0,0,1]
	v_cvt_pk_fp8_f32 v77, v16, v17 op_sel:[0,0,1]
	v_cvt_pk_fp8_f32 v78, v8, v9 op_sel:[0,0,1]
	v_cvt_pk_fp8_f32 v79, v4, v5 op_sel:[0,0,1]
	v_pk_mul_f32 v[20:21], v[72:73], s[2:3] op_sel_hi:[1,0]
	v_pk_mul_f32 v[28:29], v[28:29], s[2:3] op_sel_hi:[1,0]
	v_pk_mul_f32 v[34:35], v[34:35], s[2:3] op_sel_hi:[1,0]
	v_cvt_pk_fp8_f32 v81, v28, v29 op_sel:[0,0,1]
	v_cvt_pk_fp8_f32 v80, v34, v35 op_sel:[0,0,1]
	v_cvt_pk_fp8_f32 v82, v20, v21 op_sel:[0,0,1]
	v_cvt_pk_fp8_f32 v83, v10, v11 op_sel:[0,0,1]
	v_lshl_or_b32 v2, v18, 7, v1
	v_lshl_add_u64 v[72:73], v[2:3], 4, s[8:9]
	v_or_b32_e32 v2, v69, v74
	global_store_dwordx4 v[72:73], v[76:79], off sc1
	global_store_dwordx4 v[72:73], v[80:83], off offset:1024 sc1
	s_and_saveexec_b64 s[2:3], vcc
	s_cbranch_execz .LBB0_18
	s_mov_b64 s[8:9], s[26:27]
	v_add_f32_e32 v69, v70, v71
	v_mul_f32_e32 v69, 0x3fb8aa3b, v69
	s_waitcnt lgkmcnt(0)
	v_lshl_add_u64 v[70:71], v[2:3], 2, s[8:9]
	global_store_dword v[70:71], v69, off sc1
.LBB0_18:
	s_or_b64 exec, exec, s[2:3]
	v_fma_f32 v44, v44, v44, 0
	v_fma_f32 v3, v30, v30, 0
	v_fmac_f32_e32 v44, v43, v43
	v_fmac_f32_e32 v3, v31, v31
	v_fmac_f32_e32 v44, v42, v42
	v_fmac_f32_e32 v3, v26, v26
	v_fmac_f32_e32 v44, v41, v41
	v_fmac_f32_e32 v3, v27, v27
	v_fmac_f32_e32 v44, v40, v40
	v_fmac_f32_e32 v3, v22, v22
	v_fmac_f32_e32 v44, v38, v38
	v_fmac_f32_e32 v3, v23, v23
	v_fmac_f32_e32 v44, v19, v19
	v_fmac_f32_e32 v3, v16, v16
	v_fmac_f32_e32 v44, v39, v39
	v_fmac_f32_e32 v3, v17, v17
	v_fmac_f32_e32 v44, v52, v52
	v_fmac_f32_e32 v3, v12, v12
	v_fmac_f32_e32 v44, v51, v51
	v_fmac_f32_e32 v3, v13, v13
	v_fmac_f32_e32 v44, v50, v50
	v_fmac_f32_e32 v3, v8, v8
	v_fmac_f32_e32 v44, v49, v49
	v_fmac_f32_e32 v3, v9, v9
	v_fmac_f32_e32 v44, v48, v48
	v_fmac_f32_e32 v3, v6, v6
	v_fmac_f32_e32 v44, v46, v46
	v_fmac_f32_e32 v3, v7, v7
	v_fmac_f32_e32 v44, v45, v45
	v_fmac_f32_e32 v3, v4, v4
	v_fmac_f32_e32 v44, v47, v47
	v_fmac_f32_e32 v3, v5, v5
	v_fmac_f32_e32 v44, v60, v60
	v_fmac_f32_e32 v3, v36, v36
	v_fmac_f32_e32 v44, v59, v59
	v_fmac_f32_e32 v3, v37, v37
	v_fmac_f32_e32 v44, v58, v58
	v_fmac_f32_e32 v3, v34, v34
	v_fmac_f32_e32 v44, v57, v57
	v_fmac_f32_e32 v3, v35, v35
	v_fmac_f32_e32 v44, v56, v56
	v_fmac_f32_e32 v3, v32, v32
	v_fmac_f32_e32 v44, v54, v54
	v_fmac_f32_e32 v3, v33, v33
	v_fmac_f32_e32 v44, v53, v53
	v_fmac_f32_e32 v3, v28, v28
	v_fmac_f32_e32 v44, v55, v55
	v_fmac_f32_e32 v3, v29, v29
	v_fmac_f32_e32 v44, v68, v68
	v_fmac_f32_e32 v3, v24, v24
	v_fmac_f32_e32 v44, v67, v67
	v_fmac_f32_e32 v3, v25, v25
	v_fmac_f32_e32 v44, v66, v66
	v_fmac_f32_e32 v3, v20, v20
	v_fmac_f32_e32 v44, v65, v65
	v_fmac_f32_e32 v3, v21, v21
	v_fmac_f32_e32 v44, v64, v64
	v_fmac_f32_e32 v3, v14, v14
	v_fmac_f32_e32 v44, v62, v62
	v_fmac_f32_e32 v3, v15, v15
	v_fmac_f32_e32 v44, v61, v61
	v_fmac_f32_e32 v3, v10, v10
	v_fmac_f32_e32 v44, v63, v63
	v_fmac_f32_e32 v3, v11, v11
	v_mov_b32_e32 v5, v3
	v_mov_b32_e32 v4, v44
	s_nop 0
	v_permlane32_swap_b32_e32 v3, v5
	v_permlane32_swap_b32_e32 v44, v4
	s_and_saveexec_b64 s[8:9], vcc
	s_cbranch_execz .LBB0_20
	v_add_f32_e32 v3, v3, v5
	s_mov_b32 s10, 0xf800000
	v_mul_f32_e32 v5, 0x4f800000, v3
	v_cmp_gt_f32_e32 vcc, s10, v3
	s_mov_b64 s[2:3], s[28:29]
	s_nop 0
	v_cndmask_b32_e32 v5, v3, v5, vcc
	v_sqrt_f32_e32 v6, v5
	v_mov_b32_e32 v3, 0
	s_waitcnt lgkmcnt(0)
	v_lshl_add_u64 v[2:3], v[2:3], 2, s[2:3]
	v_add_u32_e32 v7, -1, v6
	v_fma_f32 v8, -v7, v6, v5
	v_cmp_ge_f32_e64 s[2:3], 0, v8
	v_add_u32_e32 v8, 1, v6
	s_nop 0
	v_cndmask_b32_e64 v7, v6, v7, s[2:3]
	v_fma_f32 v6, -v8, v6, v5
	v_cmp_lt_f32_e64 s[2:3], 0, v6
	s_nop 1
	v_cndmask_b32_e64 v6, v7, v8, s[2:3]
	v_mul_f32_e32 v7, 0x37800000, v6
	v_cndmask_b32_e32 v6, v6, v7, vcc
	v_mov_b32_e32 v7, 0x260
	v_cmp_class_f32_e32 vcc, v5, v7
	s_nop 1
	v_cndmask_b32_e32 v5, v6, v5, vcc
	global_store_dword v[2:3], v5, off sc1
.LBB0_20:
	s_or_b64 exec, exec, s[8:9]
	v_mbcnt_lo_u32_b32 v3, -1, 0
	v_mbcnt_hi_u32_b32 v3, -1, v3
	v_add_f32_e32 v2, v44, v4
	v_and_b32_e32 v4, 64, v3
	v_add_u32_e32 v4, 64, v4
	v_xor_b32_e32 v5, 16, v3
	v_cmp_lt_i32_e32 vcc, v5, v4
	v_xor_b32_e32 v6, 8, v3
	s_nop 0
	v_cndmask_b32_e32 v5, v3, v5, vcc
	v_lshlrev_b32_e32 v5, 2, v5
	ds_bpermute_b32 v5, v5, v2
	v_cmp_lt_i32_e32 vcc, v6, v4
	s_waitcnt lgkmcnt(0)
	v_max_f32_e32 v5, v5, v5
	v_max_f32_e32 v2, v2, v5
	v_cndmask_b32_e32 v5, v3, v6, vcc
	v_lshlrev_b32_e32 v5, 2, v5
	ds_bpermute_b32 v5, v5, v2
	v_xor_b32_e32 v6, 4, v3
	v_cmp_lt_i32_e32 vcc, v6, v4
	s_waitcnt lgkmcnt(0)
	v_max_f32_e32 v5, v5, v5
	v_max_f32_e32 v2, v2, v5
	v_cndmask_b32_e32 v5, v3, v6, vcc
	v_lshlrev_b32_e32 v5, 2, v5
	ds_bpermute_b32 v5, v5, v2
	v_xor_b32_e32 v6, 2, v3
	v_cmp_lt_i32_e32 vcc, v6, v4
	s_waitcnt lgkmcnt(0)
	v_max_f32_e32 v5, v5, v5
	v_max_f32_e32 v2, v2, v5
	v_cndmask_b32_e32 v5, v3, v6, vcc
	v_lshlrev_b32_e32 v5, 2, v5
	ds_bpermute_b32 v5, v5, v2
	v_xor_b32_e32 v6, 1, v3
	v_cmp_lt_i32_e32 vcc, v6, v4
	s_waitcnt lgkmcnt(0)
	v_max_f32_e32 v5, v5, v5
	v_cndmask_b32_e32 v3, v3, v6, vcc
	v_max_f32_e32 v2, v2, v5
	v_lshlrev_b32_e32 v3, 2, v3
	ds_bpermute_b32 v3, v3, v2
	v_cmp_eq_u32_e32 vcc, 0, v1
	s_and_saveexec_b64 s[2:3], vcc
	s_cbranch_execz .LBB0_22
	s_mov_b64 s[8:9], s[30:31]
	s_waitcnt lgkmcnt(0)
	v_max_f32_e32 v3, v3, v3
	v_max_f32_e32 v2, v2, v2
	v_mov_b32_e32 v19, 0
	v_max_f32_e32 v4, v2, v3
	v_lshl_add_u64 v[2:3], v[18:19], 2, s[8:9]
	global_store_dword v[2:3], v4, off sc1

	.amdhsa_kernel _Z11prep_kernelPKfS0_S0_S0_S0_S0_S0_PDv4_jS2_S2_PfS3_S3_S3_
		.amdhsa_group_segment_fixed_size 18944
		.amdhsa_private_segment_fixed_size 0
		.amdhsa_kernarg_size 112
		.amdhsa_user_sgpr_count 2
		.amdhsa_user_sgpr_dispatch_ptr 0
		.amdhsa_user_sgpr_queue_ptr 0
		.amdhsa_user_sgpr_kernarg_segment_ptr 1
		.amdhsa_user_sgpr_dispatch_id 0
		.amdhsa_user_sgpr_kernarg_preload_length 0
		.amdhsa_user_sgpr_kernarg_preload_offset 0
		.amdhsa_user_sgpr_private_segment_size 0
		.amdhsa_uses_dynamic_stack 0
		.amdhsa_enable_private_segment 0
		.amdhsa_system_sgpr_workgroup_id_x 1
		.amdhsa_system_sgpr_workgroup_id_y 0
		.amdhsa_system_sgpr_workgroup_id_z 0
		.amdhsa_system_sgpr_workgroup_info 0
		.amdhsa_system_vgpr_workitem_id 0
		.amdhsa_next_free_vgpr 132
		.amdhsa_next_free_sgpr 32
		.amdhsa_accum_offset 100
		.amdhsa_reserve_vcc 1
		.amdhsa_float_round_mode_32 0
		.amdhsa_float_round_mode_16_64 0
		.amdhsa_float_denorm_mode_32 3
		.amdhsa_float_denorm_mode_16_64 3
		.amdhsa_dx10_clamp 1
		.amdhsa_ieee_mode 1
		.amdhsa_fp16_overflow 0
		.amdhsa_tg_split 0
		.amdhsa_exception_fp_ieee_invalid_op 0
		.amdhsa_exception_fp_denorm_src 0
		.amdhsa_exception_fp_ieee_div_zero 0
		.amdhsa_exception_fp_ieee_overflow 0
		.amdhsa_exception_fp_ieee_underflow 0
		.amdhsa_exception_fp_ieee_inexact 0
		.amdhsa_exception_int_div_zero 0
	.end_amdhsa_kernel

.LBB1_11:
	s_lshl_b32 s0, s30, 5
	s_lshl_b32 s1, s31, 7
	s_and_b32 s13, s2, 3
	s_or_b32 s14, s0, s1
	s_lshl_b32 s0, s3, 5
	s_lshl_b32 s12, s13, 6
	s_add_i32 s1, s0, s12
	v_or_b32_e32 v36, s1, v172
	v_mov_b32_e32 v37, 0
	s_lshl_b32 s2, s13, 8
	v_lshlrev_b64 v[0:1], 8, v[36:37]
	s_add_u32 s2, s6, s2
	v_lshl_add_u64 v[0:1], s[4:5], 0, v[0:1]
	v_lshlrev_b32_e32 v36, 4, v175
	s_addc_u32 s4, s7, 0
	s_lshl_b32 s3, s3, 7
	v_lshl_add_u64 v[8:9], v[0:1], 0, v[36:37]
	s_add_u32 s2, s2, s3
	s_addc_u32 s3, s4, 0
	v_lshl_add_u64 v[10:11], v[8:9], 0, 32
	v_lshl_add_u64 v[10:11], s[2:3], 0, v[36:37]
	v_lshl_add_u64 v[12:13], v[8:9], 0, 64
	s_mov_b64 s[2:3], 0x60
	v_lshl_add_u64 v[12:13], v[8:9], 0, s[2:3]
	v_lshl_add_u64 v[12:13], v[10:11], 0, 32
	s_mov_b64 s[4:5], 0x80
	v_lshl_add_u64 v[12:13], v[8:9], 0, s[4:5]
	s_mov_b64 s[4:5], 0xa0
	v_lshl_add_u64 v[12:13], v[8:9], 0, s[4:5]
	v_lshl_add_u64 v[12:13], v[10:11], 0, 64
	s_mov_b64 s[4:5], 0xc0
	v_lshl_add_u64 v[12:13], v[8:9], 0, s[4:5]
	s_mov_b64 s[4:5], 0xe0
	v_lshl_add_u64 v[8:9], v[8:9], 0, s[4:5]
	v_lshl_add_u64 v[8:9], v[10:11], 0, s[2:3]
	s_lshl_b32 s2, s28, 20
	s_mov_b32 s1, 0
	s_add_u32 s4, s18, s2
	s_addc_u32 s5, s19, 0
	s_lshl_b64 s[2:3], s[0:1], 14
	s_add_u32 s4, s4, s2
	s_mov_b32 s15, s1
	s_addc_u32 s5, s5, s3
	s_lshl_b64 s[2:3], s[14:15], 2
	s_add_u32 s4, s4, s2
	s_addc_u32 s5, s5, s3
	v_lshlrev_b32_e32 v36, 2, v172
	v_lshl_add_u64 v[8:9], s[4:5], 0, v[36:37]
	v_lshlrev_b32_e32 v122, 16, v175
	v_mov_b32_e32 v123, v37
	v_lshl_add_u64 v[8:9], v[8:9], 0, v[122:123]
	s_mov_b64 s[4:5], 0x4000
	global_load_dword v140, v[8:9], off
	v_lshl_add_u64 v[10:11], v[8:9], 0, s[4:5]
	s_mov_b64 s[4:5], 0x8000
	global_load_dword v139, v[10:11], off
	v_lshl_add_u64 v[10:11], v[8:9], 0, s[4:5]
	s_mov_b64 s[4:5], 0xc000
	global_load_dword v138, v[10:11], off
	v_lshl_add_u64 v[10:11], v[8:9], 0, s[4:5]
	s_mov_b64 s[4:5], 0x20000
	global_load_dword v137, v[10:11], off
	v_lshl_add_u64 v[10:11], v[8:9], 0, s[4:5]
	s_mov_b64 s[4:5], 0x24000
	global_load_dword v136, v[10:11], off
	v_lshl_add_u64 v[10:11], v[8:9], 0, s[4:5]
	s_mov_b64 s[4:5], 0x28000
	global_load_dword v135, v[10:11], off
	v_lshl_add_u64 v[10:11], v[8:9], 0, s[4:5]
	s_mov_b64 s[4:5], 0x2c000
	global_load_dword v134, v[10:11], off
	v_lshl_add_u64 v[10:11], v[8:9], 0, s[4:5]
	s_mov_b64 s[4:5], 0x40000
	global_load_dword v133, v[10:11], off
	v_lshl_add_u64 v[10:11], v[8:9], 0, s[4:5]
	s_mov_b64 s[4:5], 0x44000
	global_load_dword v132, v[10:11], off
	v_lshl_add_u64 v[10:11], v[8:9], 0, s[4:5]
	s_mov_b64 s[4:5], 0x48000
	global_load_dword v131, v[10:11], off
	v_lshl_add_u64 v[10:11], v[8:9], 0, s[4:5]
	s_mov_b64 s[4:5], 0x4c000
	global_load_dword v130, v[10:11], off
	v_lshl_add_u64 v[10:11], v[8:9], 0, s[4:5]
	s_mov_b64 s[4:5], 0x60000
	global_load_dword v129, v[10:11], off
	v_lshl_add_u64 v[10:11], v[8:9], 0, s[4:5]
	s_mov_b64 s[4:5], 0x64000
	global_load_dword v128, v[10:11], off
	v_lshl_add_u64 v[10:11], v[8:9], 0, s[4:5]
	s_mov_b64 s[4:5], 0x68000
	global_load_dword v127, v[10:11], off
	v_lshl_add_u64 v[10:11], v[8:9], 0, s[4:5]
	s_mov_b64 s[4:5], 0x6c000
	v_lshl_add_u64 v[8:9], v[8:9], 0, s[4:5]
	s_lshl_b32 s4, s13, 2
	s_add_u32 s4, s8, s4
	global_load_dword v126, v[10:11], off
	s_addc_u32 s5, s9, 0
	global_load_dword v124, v[8:9], off
	v_mov_b64_e32 v[8:9], s[4:5]
	s_mul_i32 s4, s29, 0x2200
	s_add_i32 s4, s4, 0
	v_mov_b32_e32 v8, v141
	v_add_u32_e32 v9, s4, v173
	s_xor_b32 s4, s29, 4
	v_permlane32_swap_b32_e32 v141, v8
	s_mulk_i32 s4, 0x2200
	v_add_f32_e32 v8, v141, v8
	s_add_i32 s4, s4, 0
	ds_write2st64_b32 v9, v146, v8 offset1:1
	ds_write2st64_b32 v9, v54, v55 offset0:2 offset1:3
	ds_write2st64_b32 v9, v38, v39 offset0:18 offset1:19
	ds_write2st64_b32 v9, v56, v57 offset0:4 offset1:5
	ds_write2st64_b32 v9, v40, v41 offset0:20 offset1:21
	ds_write2st64_b32 v9, v58, v59 offset0:6 offset1:7
	ds_write2st64_b32 v9, v42, v43 offset0:22 offset1:23
	ds_write2st64_b32 v9, v60, v61 offset0:8 offset1:9
	ds_write2st64_b32 v9, v44, v45 offset0:24 offset1:25
	ds_write2st64_b32 v9, v62, v63 offset0:10 offset1:11
	ds_write2st64_b32 v9, v46, v47 offset0:26 offset1:27
	ds_write2st64_b32 v9, v64, v65 offset0:12 offset1:13
	ds_write2st64_b32 v9, v48, v49 offset0:28 offset1:29
	ds_write2st64_b32 v9, v66, v67 offset0:14 offset1:15
	ds_write2st64_b32 v9, v50, v51 offset0:30 offset1:31
	ds_write2st64_b32 v9, v68, v69 offset0:16 offset1:17
	ds_write2st64_b32 v9, v52, v53 offset0:32 offset1:33
	v_add_u32_e32 v66, s4, v173
	s_waitcnt lgkmcnt(0)
	s_barrier
	ds_read2st64_b32 v[10:11], v66 offset1:1
	ds_read2st64_b32 v[12:13], v66 offset0:2 offset1:3
	ds_read2st64_b32 v[14:15], v66 offset0:4 offset1:5
	ds_read2st64_b32 v[38:39], v66 offset0:6 offset1:7
	v_max_f32_e32 v40, v146, v146
	s_waitcnt lgkmcnt(3)
	v_max_f32_e32 v9, v10, v10
	v_max_f32_e32 v9, v40, v9
	v_sub_f32_e32 v40, v146, v9
	v_sub_f32_e32 v9, v10, v9
	v_exp_f32_e32 v40, v40
	v_exp_f32_e32 v41, v9
	v_mov_b32_e32 v9, v11
	v_pk_mul_f32 v[8:9], v[8:9], v[40:41]
	s_nop 0
	v_add_f32_e32 v8, v8, v9
	v_div_scale_f32 v9, s[4:5], v8, v8, 1.0
	v_rcp_f32_e32 v10, v9
	s_nop 0
	v_fma_f32 v11, -v9, v10, 1.0
	v_fmac_f32_e32 v10, v11, v10
	v_div_scale_f32 v11, vcc, 1.0, v8, 1.0
	v_mul_f32_e32 v42, v11, v10
	v_fma_f32 v43, -v9, v42, v11
	v_fmac_f32_e32 v42, v43, v10
	v_fma_f32 v9, -v9, v42, v11
	v_div_fmas_f32 v9, v9, v10, v42
	v_div_fixup_f32 v9, v9, v8, 1.0
	v_mul_f32_e32 v8, v40, v9
	v_mul_f32_e32 v10, v41, v9
	ds_read2st64_b32 v[40:41], v66 offset0:18 offset1:19
	ds_read2st64_b32 v[42:43], v66 offset0:20 offset1:21
	ds_read2st64_b32 v[44:45], v66 offset0:22 offset1:23
	ds_read2st64_b32 v[46:47], v66 offset0:16 offset1:17
	s_waitcnt lgkmcnt(6)
	v_pk_mul_f32 v[12:13], v[10:11], v[12:13] op_sel_hi:[0,1]
	s_waitcnt lgkmcnt(5)
	v_pk_mul_f32 v[14:15], v[10:11], v[14:15] op_sel_hi:[0,1]
	s_waitcnt lgkmcnt(4)
	v_pk_mul_f32 v[38:39], v[10:11], v[38:39] op_sel_hi:[0,1]
	s_waitcnt lgkmcnt(3)
	v_pk_mul_f32 v[40:41], v[10:11], v[40:41] op_sel_hi:[0,1]
	v_pk_fma_f32 v[48:49], v[8:9], v[70:71], v[40:41] op_sel_hi:[0,1,1]
	s_waitcnt lgkmcnt(2)
	v_pk_mul_f32 v[40:41], v[10:11], v[42:43] op_sel_hi:[0,1]
	v_pk_fma_f32 v[50:51], v[8:9], v[72:73], v[40:41] op_sel_hi:[0,1,1]
	s_waitcnt lgkmcnt(1)
	v_pk_mul_f32 v[40:41], v[10:11], v[44:45] op_sel_hi:[0,1]
	v_pk_fma_f32 v[52:53], v[8:9], v[74:75], v[40:41] op_sel_hi:[0,1,1]
	ds_read2st64_b32 v[40:41], v66 offset0:8 offset1:9
	ds_read2st64_b32 v[42:43], v66 offset0:24 offset1:25
	ds_read2st64_b32 v[44:45], v66 offset0:10 offset1:11
	ds_read2st64_b32 v[54:55], v66 offset0:12 offset1:13
	ds_read2st64_b32 v[56:57], v66 offset0:14 offset1:15
	ds_read2st64_b32 v[58:59], v66 offset0:26 offset1:27
	ds_read2st64_b32 v[60:61], v66 offset0:28 offset1:29
	ds_read2st64_b32 v[62:63], v66 offset0:30 offset1:31
	s_waitcnt lgkmcnt(6)
	v_pk_mul_f32 v[42:43], v[10:11], v[42:43] op_sel_hi:[0,1]
	v_pk_fma_f32 v[64:65], v[8:9], v[76:77], v[42:43] op_sel_hi:[0,1,1]
	s_waitcnt lgkmcnt(5)
	v_pk_mul_f32 v[42:43], v[10:11], v[44:45] op_sel_hi:[0,1]
	s_waitcnt lgkmcnt(2)
	v_pk_mul_f32 v[44:45], v[10:11], v[58:59] op_sel_hi:[0,1]
	v_pk_fma_f32 v[58:59], v[8:9], v[78:79], v[44:45] op_sel_hi:[0,1,1]
	v_pk_mul_f32 v[44:45], v[10:11], v[54:55] op_sel_hi:[0,1]
	s_waitcnt lgkmcnt(1)
	v_pk_mul_f32 v[54:55], v[10:11], v[60:61] op_sel_hi:[0,1]
	ds_read2st64_b32 v[60:61], v66 offset0:32 offset1:33
	s_waitcnt vmcnt(0)
	v_pk_mul_f32 v[40:41], v[10:11], v[40:41] op_sel_hi:[0,1]
	v_cvt_pk_bf16_f32 v0, v208, v209
	v_cvt_pk_bf16_f32 v1, v210, v211
	v_cvt_pk_bf16_f32 v2, v212, v213
	v_cvt_pk_bf16_f32 v3, v214, v215
	v_pk_fma_f32 v[12:13], v[8:9], v[86:87], v[12:13] op_sel_hi:[0,1,1]
	v_pk_fma_f32 v[14:15], v[8:9], v[88:89], v[14:15] op_sel_hi:[0,1,1]
	v_pk_fma_f32 v[38:39], v[8:9], v[90:91], v[38:39] op_sel_hi:[0,1,1]
	v_pk_fma_f32 v[40:41], v[8:9], v[92:93], v[40:41] op_sel_hi:[0,1,1]
	v_pk_mul_f32 v[56:57], v[10:11], v[56:57] op_sel_hi:[0,1]
	s_waitcnt lgkmcnt(1)
	v_pk_mul_f32 v[62:63], v[10:11], v[62:63] op_sel_hi:[0,1]
	v_pk_mul_f32 v[46:47], v[10:11], v[46:47] op_sel_hi:[0,1]
	s_waitcnt lgkmcnt(0)
	v_pk_mul_f32 v[10:11], v[10:11], v[60:61] op_sel_hi:[0,1]
	v_cvt_pk_bf16_f32 v4, v12, v13
	v_cvt_pk_bf16_f32 v5, v14, v15
	v_cvt_pk_bf16_f32 v6, v38, v39
	v_cvt_pk_bf16_f32 v7, v40, v41
	v_pk_fma_f32 v[42:43], v[8:9], v[94:95], v[42:43] op_sel_hi:[0,1,1]
	v_pk_fma_f32 v[44:45], v[8:9], v[96:97], v[44:45] op_sel_hi:[0,1,1]
	v_pk_fma_f32 v[54:55], v[8:9], v[80:81], v[54:55] op_sel_hi:[0,1,1]
	v_pk_fma_f32 v[56:57], v[8:9], v[98:99], v[56:57] op_sel_hi:[0,1,1]
	v_pk_fma_f32 v[62:63], v[8:9], v[82:83], v[62:63] op_sel_hi:[0,1,1]
	v_pk_fma_f32 v[46:47], v[8:9], v[100:101], v[46:47] op_sel_hi:[0,1,1]
	v_pk_fma_f32 v[60:61], v[8:9], v[84:85], v[10:11] op_sel_hi:[0,1,1]
	v_mfma_f32_32x32x16_bf16 v[0:15], v[0:3], v[4:7], 0
	v_cvt_pk_bf16_f32 v42, v42, v43
	v_cvt_pk_bf16_f32 v38, v216, v217
	v_cvt_pk_bf16_f32 v39, v218, v219
	v_cvt_pk_bf16_f32 v40, v220, v221
	v_cvt_pk_bf16_f32 v41, v222, v223
	v_cvt_pk_bf16_f32 v43, v44, v45
	v_cvt_pk_bf16_f32 v44, v56, v57
	v_cvt_pk_bf16_f32 v45, v46, v47
	s_nop 1
	v_mfma_f32_32x32x16_bf16 v[0:15], v[38:41], v[42:45], v[0:15]
	v_cvt_pk_bf16_f32 v38, v224, v225
	v_cvt_pk_bf16_f32 v39, v226, v227
	v_cvt_pk_bf16_f32 v40, v228, v229
	v_cvt_pk_bf16_f32 v41, v230, v231
	v_cvt_pk_bf16_f32 v42, v48, v49
	v_cvt_pk_bf16_f32 v43, v50, v51
	v_cvt_pk_bf16_f32 v44, v52, v53
	v_cvt_pk_bf16_f32 v45, v64, v65
	v_cvt_pk_bf16_f32 v32, v232, v233
	v_cvt_pk_bf16_f32 v33, v234, v235
	v_mfma_f32_32x32x16_bf16 v[0:15], v[38:41], v[42:45], v[0:15]
	v_cvt_pk_bf16_f32 v34, v236, v237
	v_cvt_pk_bf16_f32 v35, v238, v239
	v_cvt_pk_bf16_f32 v38, v58, v59
	v_add_f32_e32 v42, 1.0, v205
	v_div_scale_f32 v43, s[4:5], v42, v42, 1.0
	v_rcp_f32_e32 v44, v43
	v_cvt_pk_bf16_f32 v39, v54, v55
	v_cvt_pk_bf16_f32 v40, v62, v63
	v_cvt_pk_bf16_f32 v41, v60, v61
	s_lshl_b32 s4, s28, 8
	s_or_b32 s4, s4, s12
	v_mfma_f32_32x32x16_bf16 v[0:15], v[32:35], v[38:41], v[0:15]
	v_fma_f32 v32, -v43, v44, 1.0
	v_fmac_f32_e32 v44, v32, v44
	v_div_scale_f32 v32, vcc, 1.0, v42, 1.0
	s_add_i32 s0, s4, s0
	v_mul_f32_e32 v33, v32, v44
	s_lshl_b64 s[0:1], s[0:1], 14
	v_fma_f32 v34, -v43, v33, v32
	s_add_u32 s0, s10, s0
	v_fmac_f32_e32 v33, v34, v44
	s_addc_u32 s1, s11, s1
	v_fma_f32 v32, -v43, v33, v32
	s_add_u32 s0, s0, s2
	v_div_fmas_f32 v32, v32, v44, v33
	s_addc_u32 s1, s1, s3
	v_add_f32_e32 v0, v0, v240
	v_div_fixup_f32 v34, v32, v42, 1.0
	v_lshl_add_u64 v[32:33], s[0:1], 0, v[36:37]
	v_fmac_f32_e32 v140, v205, v0
	v_mul_f32_e32 v0, v34, v140
	v_lshl_add_u64 v[32:33], v[32:33], 0, v[122:123]
	global_store_dword v[32:33], v0, off sc1
	v_add_f32_e32 v0, v1, v241
	s_movk_i32 s0, 0x4000
	v_fmac_f32_e32 v139, v205, v0
	v_add_co_u32_e32 v0, vcc, s0, v32
	v_mul_f32_e32 v28, v34, v139
	s_nop 0
	v_addc_co_u32_e32 v1, vcc, 0, v33, vcc
	global_store_dword v[0:1], v28, off sc1
	v_add_f32_e32 v0, v2, v242
	s_mov_b32 s0, 0x8000
	v_fmac_f32_e32 v138, v205, v0
	v_add_co_u32_e32 v0, vcc, s0, v32
	v_mul_f32_e32 v2, v34, v138
	s_nop 0
	v_addc_co_u32_e32 v1, vcc, 0, v33, vcc
	global_store_dword v[0:1], v2, off sc1
	v_add_f32_e32 v0, v3, v243
	s_mov_b32 s0, 0xc000
	v_fmac_f32_e32 v137, v205, v0
	v_add_co_u32_e32 v0, vcc, s0, v32
	v_mul_f32_e32 v2, v34, v137
	s_nop 0
	v_addc_co_u32_e32 v1, vcc, 0, v33, vcc
	global_store_dword v[0:1], v2, off sc1
	v_add_f32_e32 v0, v4, v244
	s_mov_b32 s0, 0x20000
	v_fmac_f32_e32 v136, v205, v0
	v_add_co_u32_e32 v0, vcc, s0, v32
	v_mul_f32_e32 v2, v34, v136
	s_nop 0
	v_addc_co_u32_e32 v1, vcc, 0, v33, vcc
	global_store_dword v[0:1], v2, off sc1
	v_add_f32_e32 v0, v5, v245
	s_mov_b32 s0, 0x24000
	v_fmac_f32_e32 v135, v205, v0
	v_add_co_u32_e32 v0, vcc, s0, v32
	v_mul_f32_e32 v2, v34, v135
	s_nop 0
	v_addc_co_u32_e32 v1, vcc, 0, v33, vcc
	global_store_dword v[0:1], v2, off sc1
	v_add_f32_e32 v0, v6, v246
	s_mov_b32 s0, 0x28000
	v_fmac_f32_e32 v134, v205, v0
	v_add_co_u32_e32 v0, vcc, s0, v32
	v_mul_f32_e32 v2, v34, v134
	s_nop 0
	v_addc_co_u32_e32 v1, vcc, 0, v33, vcc
	global_store_dword v[0:1], v2, off sc1
	v_add_f32_e32 v0, v7, v247
	s_mov_b32 s0, 0x2c000
	v_fmac_f32_e32 v133, v205, v0
	v_add_co_u32_e32 v0, vcc, s0, v32
	v_mul_f32_e32 v2, v34, v133
	s_nop 0
	v_addc_co_u32_e32 v1, vcc, 0, v33, vcc
	global_store_dword v[0:1], v2, off sc1
	v_add_f32_e32 v0, v8, v248
	s_mov_b32 s0, 0x40000
	v_fmac_f32_e32 v132, v205, v0
	v_add_co_u32_e32 v0, vcc, s0, v32
	v_mul_f32_e32 v2, v34, v132
	s_nop 0
	v_addc_co_u32_e32 v1, vcc, 0, v33, vcc
	global_store_dword v[0:1], v2, off sc1
	v_add_f32_e32 v0, v9, v249
	s_mov_b32 s0, 0x44000
	v_fmac_f32_e32 v131, v205, v0
	v_add_co_u32_e32 v0, vcc, s0, v32
	v_mul_f32_e32 v2, v34, v131
	s_nop 0
	v_addc_co_u32_e32 v1, vcc, 0, v33, vcc
	global_store_dword v[0:1], v2, off sc1
	v_add_f32_e32 v0, v10, v250
	s_mov_b32 s0, 0x48000
	v_fmac_f32_e32 v130, v205, v0
	v_add_co_u32_e32 v0, vcc, s0, v32
	v_mul_f32_e32 v2, v34, v130
	s_nop 0
	v_addc_co_u32_e32 v1, vcc, 0, v33, vcc
	global_store_dword v[0:1], v2, off sc1
	v_add_f32_e32 v0, v11, v251
	s_mov_b32 s0, 0x4c000
	v_fmac_f32_e32 v129, v205, v0
	v_add_co_u32_e32 v0, vcc, s0, v32
	v_mul_f32_e32 v2, v34, v129
	s_nop 0
	v_addc_co_u32_e32 v1, vcc, 0, v33, vcc
	global_store_dword v[0:1], v2, off sc1
	v_add_f32_e32 v0, v12, v252
	s_mov_b32 s0, 0x60000
	v_fmac_f32_e32 v128, v205, v0
	v_add_co_u32_e32 v0, vcc, s0, v32
	v_mul_f32_e32 v2, v34, v128
	s_nop 0
	v_addc_co_u32_e32 v1, vcc, 0, v33, vcc
	global_store_dword v[0:1], v2, off sc1
	v_add_f32_e32 v0, v13, v253
	s_mov_b32 s0, 0x64000
	v_fmac_f32_e32 v127, v205, v0
	v_add_co_u32_e32 v0, vcc, s0, v32
	v_mul_f32_e32 v2, v34, v127
	s_nop 0
	v_addc_co_u32_e32 v1, vcc, 0, v33, vcc
	global_store_dword v[0:1], v2, off sc1
	v_add_f32_e32 v0, v14, v254
	s_mov_b32 s0, 0x68000
	v_fmac_f32_e32 v126, v205, v0
	v_add_co_u32_e32 v0, vcc, s0, v32
	v_mul_f32_e32 v2, v34, v126
	s_nop 0
	v_addc_co_u32_e32 v1, vcc, 0, v33, vcc
	global_store_dword v[0:1], v2, off sc1
	v_add_f32_e32 v0, v15, v255
	v_fmac_f32_e32 v124, v205, v0
	v_add_co_u32_e32 v0, vcc, 0x6c000, v32
	v_mul_f32_e32 v2, v34, v124
	s_nop 0
	v_addc_co_u32_e32 v1, vcc, 0, v33, vcc
	global_store_dword v[0:1], v2, off sc1
	s_endpgm

amdhsa.kernels:
  - .agpr_count:     32
    .args:
      - .actual_access:  read_only
        .address_space:  global
        .offset:         0
        .size:           8
        .value_kind:     global_buffer
      - .actual_access:  read_only
        .address_space:  global
        .offset:         8
        .size:           8
        .value_kind:     global_buffer
      - .actual_access:  read_only
        .address_space:  global
        .offset:         16
        .size:           8
        .value_kind:     global_buffer
      - .actual_access:  read_only
        .address_space:  global
        .offset:         24
        .size:           8
        .value_kind:     global_buffer
      - .actual_access:  read_only
        .address_space:  global
        .offset:         32
        .size:           8
        .value_kind:     global_buffer
      - .actual_access:  read_only
        .address_space:  global
        .offset:         40
        .size:           8
        .value_kind:     global_buffer
      - .actual_access:  read_only
        .address_space:  global
        .offset:         48
        .size:           8
        .value_kind:     global_buffer
      - .actual_access:  write_only
        .address_space:  global
        .offset:         56
        .size:           8
        .value_kind:     global_buffer
      - .actual_access:  write_only
        .address_space:  global
        .offset:         64
        .size:           8
        .value_kind:     global_buffer
      - .actual_access:  write_only
        .address_space:  global
        .offset:         72
        .size:           8
        .value_kind:     global_buffer
      - .actual_access:  write_only
        .address_space:  global
        .offset:         80
        .size:           8
        .value_kind:     global_buffer
      - .actual_access:  write_only
        .address_space:  global
        .offset:         88
        .size:           8
        .value_kind:     global_buffer
      - .actual_access:  write_only
        .address_space:  global
        .offset:         96
        .size:           8
        .value_kind:     global_buffer
      - .actual_access:  write_only
        .address_space:  global
        .offset:         104
        .size:           8
        .value_kind:     global_buffer
    .group_segment_fixed_size: 18944
    .kernarg_segment_align: 8
    .kernarg_segment_size: 112
    .language:       OpenCL C
    .language_version:
      - 2
      - 0
    .max_flat_workgroup_size: 256
    .name:           _Z11prep_kernelPKfS0_S0_S0_S0_S0_S0_PDv4_jS2_S2_PfS3_S3_S3_
    .private_segment_fixed_size: 0
    .sgpr_count:     38
    .sgpr_spill_count: 0
    .symbol:         _Z11prep_kernelPKfS0_S0_S0_S0_S0_S0_PDv4_jS2_S2_PfS3_S3_S3_.kd
    .uniform_work_group_size: 1
    .uses_dynamic_stack: false
    .vgpr_count:     132
    .vgpr_spill_count: 0
    .wavefront_size: 64
  - .agpr_count:     0
    .args:
      - .address_space:  global
        .offset:         0
        .size:           8
        .value_kind:     global_buffer
      - .address_space:  global
        .offset:         8
        .size:           8
        .value_kind:     global_buffer
      - .address_space:  global
        .offset:         16
        .size:           8
        .value_kind:     global_buffer
      - .address_space:  global
        .offset:         24
        .size:           8
        .value_kind:     global_buffer
      - .address_space:  global
        .offset:         32
        .size:           8
        .value_kind:     global_buffer
      - .actual_access:  read_only
        .address_space:  global
        .offset:         40
        .size:           8
        .value_kind:     global_buffer
      - .actual_access:  read_only
        .address_space:  global
        .offset:         48
        .size:           8
        .value_kind:     global_buffer
      - .address_space:  global
        .offset:         56
        .size:           8
        .value_kind:     global_buffer
      - .actual_access:  read_only
        .address_space:  global
        .offset:         64
        .size:           8
        .value_kind:     global_buffer
      - .actual_access:  read_only
        .address_space:  global
        .offset:         72
        .size:           8
        .value_kind:     global_buffer
      - .actual_access:  write_only
        .address_space:  global
        .offset:         80
        .size:           8
        .value_kind:     global_buffer
    .group_segment_fixed_size: 0
    .kernarg_segment_align: 8
    .kernarg_segment_size: 88
    .language:       OpenCL C
    .language_version:
      - 2
      - 0
    .max_flat_workgroup_size: 512
    .name:           _Z11attn_kernelPKfS0_S0_PKcS2_PKDv4_jS0_S0_S0_S0_Pf
    .private_segment_fixed_size: 0
    .sgpr_count:     53
    .sgpr_spill_count: 0
    .symbol:         _Z11attn_kernelPKfS0_S0_PKcS2_PKDv4_jS0_S0_S0_S0_Pf.kd
    .uniform_work_group_size: 1
    .uses_dynamic_stack: false
    .vgpr_count:     256
    .vgpr_spill_count: 0
    .wavefront_size: 64
